# MoE K loops: loop-invariant wave-uniform 'wave inactive' test (VALU->SGPR pair) hoisted out of the loop head to the unit start
# speedup vs baseline: 1.0008x; 1.0008x over previous
; #define MG_LDB(dst, b, h) do { _Pragma("unroll") for (int n = 0; n < 2; ++n) _Pragma("unroll") for (int k = 0; k < 2; ++k) dst[n][k] = *(const PG8_LAS bf16x8*)(lds + MG_SB(b, h) + boff + n * 2048 + k * 1024); } while (0)
; template <class Epi, bool G1> ...
;     ...
;         const bool has_next = S.next(ui + 1, nxt);
;         const bool wact = MG_WACT(cur);
;         for (int t = 0; t < NT; ++t) {
;             const bool last = (t == NT - 1), more = !last || has_next;
;             if (wact) { MG_LDB(B0, buf, 0); MG_LDB(B1, buf, 1); }
.LBB0_1073:
	v_mov_b32_e32 v199, v197
	v_mov_b32_e32 v193, v197
	v_mov_b32_e32 v195, v197
	s_xor_b64 s[38:39], s[40:41], -1
	v_lshl_add_u64 v[206:207], v[196:197], 0, s[30:31]
	v_lshl_add_u64 v[208:209], v[198:199], 0, s[30:31]
	v_lshl_add_u64 v[210:211], v[192:193], 0, s[30:31]
	v_lshl_add_u64 v[212:213], v[194:195], 0, s[30:31]
	v_cmp_ne_u32_e64 s[14:15], -1, v194
	v_cmp_ne_u32_e64 s[12:13], -1, v192
	v_cmp_ne_u32_e64 s[8:9], -1, v198
	v_cmp_ne_u32_e64 s[6:7], -1, v196
	v_mbcnt_lo_u32_b32 v226, -1, 0
	v_mbcnt_hi_u32_b32 v226, -1, v226
	v_lshl_add_u32 v226, v226, 4, s51
	v_mov_b32_e32 v228, 0
	v_mov_b32_e32 v229, 0
	v_mov_b32_e32 v230, 0
	v_mov_b32_e32 v231, 0
	s_andn2_b64 exec, exec, s[14:15]
	ds_write_b128 v226, v[228:231]
	ds_write_b128 v226, v[228:231] offset:32768
	s_mov_b64 exec, -1
	s_andn2_b64 exec, exec, s[12:13]
	ds_write_b128 v226, v[228:231] offset:8192
	ds_write_b128 v226, v[228:231] offset:40960
	s_mov_b64 exec, -1
	s_andn2_b64 exec, exec, s[8:9]
	ds_write_b128 v226, v[228:231] offset:16384
	ds_write_b128 v226, v[228:231] offset:49152
	s_mov_b64 exec, -1
	s_andn2_b64 exec, exec, s[6:7]
	ds_write_b128 v226, v[228:231] offset:24576
	ds_write_b128 v226, v[228:231] offset:57344
	s_mov_b64 exec, -1
	s_mov_b64 s[42:43], 0
	s_mov_b64 s[44:45], s[2:3]
	v_cndmask_b32_e64 v203, 0, 1, s[36:37]
	s_nop 0
	v_cmp_ne_u32_e64 s[10:11], 1, v203
	s_branch .LBB0_1075

; #define MG_LDB(dst, b, h) do { _Pragma("unroll") for (int n = 0; n < 2; ++n) _Pragma("unroll") for (int k = 0; k < 2; ++k) dst[n][k] = *(const PG8_LAS bf16x8*)(lds + MG_SB(b, h) + boff + n * 2048 + k * 1024); } while (0)
; template <class Epi, bool G1> ...
;     ...
;         const bool wact = MG_WACT(cur);
;         for (int t = 0; t < NT; ++t) {
;             const bool last = (t == NT - 1), more = !last || has_next;
;             if (wact) { MG_LDB(B0, buf, 0); MG_LDB(B1, buf, 1); }
.LBB0_1075:
	s_mov_b32 s70, s46
	s_andn2_b64 vcc, exec, s[36:37]
	s_lshl_b32 s71, s46, 15
	s_cbranch_vccz .LBB0_1082
	s_xor_b32 s72, s71, 0x8000
	s_and_saveexec_b64 s[46:47], s[14:15]
	s_cbranch_execnz .LBB0_1083

; template <class Epi, bool G1> ...
;     ...
;     for (;;) {
;         const bool has_next = S.next(ui + 1, nxt);
;         const bool wact = MG_WACT(cur);
.LBB0_1262:
	v_mov_b32_e32 v203, v1
	v_mov_b32_e32 v201, v1
	v_mov_b32_e32 v199, v1
	s_xor_b64 s[16:17], s[46:47], -1
	v_lshl_add_u64 v[2:3], v[0:1], 0, s[40:41]
	v_lshl_add_u64 v[208:209], v[202:203], 0, s[40:41]
	v_lshl_add_u64 v[210:211], v[200:201], 0, s[40:41]
	v_lshl_add_u64 v[212:213], v[198:199], 0, s[40:41]
	v_cmp_ne_u32_e64 s[14:15], -1, v198
	v_cmp_ne_u32_e64 s[12:13], -1, v200
	v_cmp_ne_u32_e64 s[8:9], -1, v202
	v_cmp_ne_u32_e64 s[6:7], -1, v0
	v_mbcnt_lo_u32_b32 v226, -1, 0
	v_mbcnt_hi_u32_b32 v226, -1, v226
	v_lshl_add_u32 v226, v226, 4, s57
	v_mov_b32_e32 v228, 0
	v_mov_b32_e32 v229, 0
	v_mov_b32_e32 v230, 0
	v_mov_b32_e32 v231, 0
	s_andn2_b64 exec, exec, s[14:15]
	ds_write_b128 v226, v[228:231]
	ds_write_b128 v226, v[228:231] offset:32768
	s_mov_b64 exec, -1
	s_andn2_b64 exec, exec, s[12:13]
	ds_write_b128 v226, v[228:231] offset:8192
	ds_write_b128 v226, v[228:231] offset:40960
	s_mov_b64 exec, -1
	s_andn2_b64 exec, exec, s[8:9]
	ds_write_b128 v226, v[228:231] offset:16384
	ds_write_b128 v226, v[228:231] offset:49152
	s_mov_b64 exec, -1
	s_andn2_b64 exec, exec, s[6:7]
	ds_write_b128 v226, v[228:231] offset:24576
	ds_write_b128 v226, v[228:231] offset:57344
	s_mov_b64 exec, -1
	s_mov_b64 s[48:49], 0
	s_mov_b64 s[50:51], s[18:19]
	v_cndmask_b32_e64 v205, 0, 1, s[44:45]
	s_nop 0
	v_cmp_ne_u32_e64 s[10:11], 1, v205
	s_branch .LBB0_1264

; #define MG_STAGE_A(b, rows, k0) do { _Pragma("unroll") for (int h_ = 0; h_ < 2; ++h_) _Pragma("unroll") for (int i_ = 0; i_ < 2; ++i_) if (rows[h_][i_] != 0xffffffffu) \
;         __builtin_amdgcn_global_load_lds((const unsigned*)((const char*)Abase + rows[h_][i_] + (k0) * 2), (PG8_LAS unsigned*)(lds + MG_SA(b, h_) + ldsw + i_ * 8192), 16, 0, 0); } while (0)
; #define MG_LDB(dst, b, h) do { _Pragma("unroll") for (int n = 0; n < 2; ++n) _Pragma("unroll") for (int k = 0; k < 2; ++k) dst[n][k] = *(const PG8_LAS bf16x8*)(lds + MG_SB(b, h) + boff + n * 2048 + k * 1024); } while (0)
; template <class Epi, bool G1> ...
;     ...
;         const bool wact = MG_WACT(cur);
;         for (int t = 0; t < NT; ++t) {
;             const bool last = (t == NT - 1), more = !last || has_next;
;             if (wact) { MG_LDB(B0, buf, 0); MG_LDB(B1, buf, 1); }
;             if (!last) { MG_STAGE_A(buf ^ 1, rowC, (t + 1) * BK); }
.LBB0_1264:
	s_mov_b32 s73, s52
	s_andn2_b64 vcc, exec, s[44:45]
	s_lshl_b32 s74, s52, 15
	s_cbranch_vccz .LBB0_1271
	s_xor_b32 s75, s74, 0x8000
	s_and_saveexec_b64 s[52:53], s[14:15]
	s_cbranch_execnz .LBB0_1272
